# nt (non-temporal) hint on the once-read f32 weight loads of the lora/conv phase's conversion wave (97 flat/global loads); stores and all other loads unchanged
# speedup vs baseline: 1.0082x; 1.0072x over previous
.LBB0_535:
	s_cmp_lg_u32 s5, 2
	s_cselect_b32 s10, s6, 0x800
	s_cmp_eq_u32 s5, 1
	s_cselect_b32 s7, s16, s18
	s_cselect_b32 s11, s17, s19
	s_cmp_eq_u32 s5, 0
	s_cselect_b32 s5, s15, s11
	s_cselect_b32 s11, s14, s7
	s_mul_hi_i32 s7, s9, s6
	s_mul_i32 s6, s9, s6
	s_lshl_b64 s[6:7], s[6:7], 13
	s_add_u32 s6, s11, s6
	v_and_or_b32 v1, v137, 32, s8
	s_addc_u32 s7, s5, s7
	v_mad_i64_i32 v[4:5], s[8:9], s10, v1, 0
	v_lshl_add_u64 v[4:5], v[4:5], 2, s[6:7]
	s_ashr_i32 s5, s4, 31
	v_and_b32_e32 v1, 31, v137
	v_lshl_add_u64 v[4:5], s[4:5], 2, v[4:5]
	v_lshlrev_b32_e32 v6, 2, v1
	v_mov_b32_e32 v7, v3
	v_lshl_add_u64 v[4:5], v[4:5], 0, v[6:7]
	s_lshl_b32 s92, s10, 2
	v_lshl_add_u64 v[6:7], v[4:5], 0, s[92:93]
	global_load_dword v1, v[4:5], off nt
	flat_load_dword v5, v[6:7] nt
	v_lshl_add_u64 v[8:9], v[6:7], 0, s[92:93]
	flat_load_dword v7, v[8:9] nt
	v_lshl_add_u64 v[10:11], v[8:9], 0, s[92:93]
	flat_load_dword v8, v[10:11] nt
	v_lshl_add_u64 v[10:11], v[10:11], 0, s[92:93]
	flat_load_dword v9, v[10:11] nt
	v_lshl_add_u64 v[12:13], v[10:11], 0, s[92:93]
	flat_load_dword v10, v[12:13] nt
	v_lshl_add_u64 v[12:13], v[12:13], 0, s[92:93]
	flat_load_dword v11, v[12:13] nt
	v_lshl_add_u64 v[14:15], v[12:13], 0, s[92:93]
	flat_load_dword v12, v[14:15] nt
	v_lshl_add_u64 v[14:15], v[14:15], 0, s[92:93]
	flat_load_dword v13, v[14:15] nt
	v_lshl_add_u64 v[16:17], v[14:15], 0, s[92:93]
	flat_load_dword v14, v[16:17] nt
	v_lshl_add_u64 v[16:17], v[16:17], 0, s[92:93]
	flat_load_dword v15, v[16:17] nt
	v_lshl_add_u64 v[18:19], v[16:17], 0, s[92:93]
	flat_load_dword v16, v[18:19] nt
	v_lshl_add_u64 v[18:19], v[18:19], 0, s[92:93]
	flat_load_dword v17, v[18:19] nt
	v_lshl_add_u64 v[20:21], v[18:19], 0, s[92:93]
	flat_load_dword v18, v[20:21] nt
	v_lshl_add_u64 v[20:21], v[20:21], 0, s[92:93]
	flat_load_dword v19, v[20:21] nt
	v_lshl_add_u64 v[22:23], v[20:21], 0, s[92:93]
	flat_load_dword v20, v[22:23] nt
	v_lshl_add_u64 v[22:23], v[22:23], 0, s[92:93]
	flat_load_dword v21, v[22:23] nt
	v_lshl_add_u64 v[24:25], v[22:23], 0, s[92:93]
	flat_load_dword v22, v[24:25] nt
	v_lshl_add_u64 v[24:25], v[24:25], 0, s[92:93]
	flat_load_dword v23, v[24:25] nt
	v_lshl_add_u64 v[26:27], v[24:25], 0, s[92:93]
	flat_load_dword v24, v[26:27] nt
	v_lshl_add_u64 v[26:27], v[26:27], 0, s[92:93]
	flat_load_dword v25, v[26:27] nt
	v_lshl_add_u64 v[28:29], v[26:27], 0, s[92:93]
	flat_load_dword v26, v[28:29] nt
	v_lshl_add_u64 v[28:29], v[28:29], 0, s[92:93]
	flat_load_dword v27, v[28:29] nt
	v_lshl_add_u64 v[30:31], v[28:29], 0, s[92:93]
	flat_load_dword v28, v[30:31] nt
	v_lshl_add_u64 v[30:31], v[30:31], 0, s[92:93]
	flat_load_dword v29, v[30:31] nt
	v_lshl_add_u64 v[32:33], v[30:31], 0, s[92:93]
	flat_load_dword v30, v[32:33] nt
	v_lshl_add_u64 v[32:33], v[32:33], 0, s[92:93]
	flat_load_dword v31, v[32:33] nt
	v_lshl_add_u64 v[34:35], v[32:33], 0, s[92:93]
	flat_load_dword v32, v[34:35] nt
	v_lshl_add_u64 v[34:35], v[34:35], 0, s[92:93]
	flat_load_dword v33, v[34:35] nt
	v_lshl_add_u64 v[36:37], v[34:35], 0, s[92:93]
	flat_load_dword v34, v[36:37] nt
	v_lshl_add_u64 v[36:37], v[36:37], 0, s[92:93]
	flat_load_dword v35, v[36:37] nt
	v_lshl_add_u64 v[38:39], v[36:37], 0, s[92:93]
	flat_load_dword v36, v[38:39] nt
	v_lshl_add_u64 v[38:39], v[38:39], 0, s[92:93]

.LBB0_554:
	s_cmp_lg_u32 s7, 2
	s_cselect_b32 s34, s8, 0x800
	s_cmp_eq_u32 s7, 1
	s_cselect_b32 s9, s16, s18
	s_cselect_b32 s35, s17, s19
	s_cmp_eq_u32 s7, 0
	s_cselect_b32 s7, s15, s35
	s_cselect_b32 s35, s14, s9
	s_mul_hi_i32 s9, s11, s8
	s_mul_i32 s8, s11, s8
	s_lshl_b64 s[8:9], s[8:9], 13
	s_add_u32 s8, s35, s8
	v_or_b32_e32 v37, s10, v4
	s_addc_u32 s9, s7, s9
	v_mad_i64_i32 v[38:39], s[10:11], s34, v37, 0
	v_lshl_add_u64 v[38:39], v[38:39], 2, s[8:9]
	s_ashr_i32 s7, s6, 31
	v_lshl_add_u64 v[38:39], s[6:7], 2, v[38:39]
	v_lshlrev_b32_e32 v40, 2, v6
	v_mov_b32_e32 v41, v3
	v_lshl_add_u64 v[38:39], v[38:39], 0, v[40:41]
	s_lshl_b32 s92, s34, 2
	v_lshl_add_u64 v[40:41], v[38:39], 0, s[92:93]
	global_load_dword v37, v[38:39], off nt
	flat_load_dword v38, v[40:41] nt
	v_lshl_add_u64 v[40:41], v[40:41], 0, s[92:93]
	flat_load_dword v39, v[40:41] nt
	v_lshl_add_u64 v[42:43], v[40:41], 0, s[92:93]
	flat_load_dword v40, v[42:43] nt
	v_lshl_add_u64 v[42:43], v[42:43], 0, s[92:93]
	flat_load_dword v41, v[42:43] nt
	v_lshl_add_u64 v[44:45], v[42:43], 0, s[92:93]
	flat_load_dword v42, v[44:45] nt
	v_lshl_add_u64 v[44:45], v[44:45], 0, s[92:93]
	flat_load_dword v43, v[44:45] nt
	v_lshl_add_u64 v[46:47], v[44:45], 0, s[92:93]
	flat_load_dword v44, v[46:47] nt
	v_lshl_add_u64 v[46:47], v[46:47], 0, s[92:93]
	flat_load_dword v45, v[46:47] nt
	v_lshl_add_u64 v[48:49], v[46:47], 0, s[92:93]
	flat_load_dword v46, v[48:49] nt
	v_lshl_add_u64 v[48:49], v[48:49], 0, s[92:93]
	flat_load_dword v47, v[48:49] nt
	v_lshl_add_u64 v[50:51], v[48:49], 0, s[92:93]
	flat_load_dword v48, v[50:51] nt
	v_lshl_add_u64 v[50:51], v[50:51], 0, s[92:93]
	flat_load_dword v49, v[50:51] nt
	v_lshl_add_u64 v[52:53], v[50:51], 0, s[92:93]
	flat_load_dword v50, v[52:53] nt
	v_lshl_add_u64 v[52:53], v[52:53], 0, s[92:93]
	flat_load_dword v51, v[52:53] nt
	v_lshl_add_u64 v[54:55], v[52:53], 0, s[92:93]
	flat_load_dword v52, v[54:55] nt
	v_lshl_add_u64 v[54:55], v[54:55], 0, s[92:93]
	flat_load_dword v53, v[54:55] nt
	v_lshl_add_u64 v[56:57], v[54:55], 0, s[92:93]
	flat_load_dword v54, v[56:57] nt
	v_lshl_add_u64 v[56:57], v[56:57], 0, s[92:93]
	flat_load_dword v55, v[56:57] nt
	v_lshl_add_u64 v[58:59], v[56:57], 0, s[92:93]
	flat_load_dword v56, v[58:59] nt
	v_lshl_add_u64 v[58:59], v[58:59], 0, s[92:93]
	flat_load_dword v57, v[58:59] nt
	v_lshl_add_u64 v[60:61], v[58:59], 0, s[92:93]
	flat_load_dword v58, v[60:61] nt
	v_lshl_add_u64 v[60:61], v[60:61], 0, s[92:93]
	flat_load_dword v59, v[60:61] nt
	v_lshl_add_u64 v[62:63], v[60:61], 0, s[92:93]
	flat_load_dword v60, v[62:63] nt
	v_lshl_add_u64 v[62:63], v[62:63], 0, s[92:93]
	flat_load_dword v61, v[62:63] nt
	v_lshl_add_u64 v[64:65], v[62:63], 0, s[92:93]
	flat_load_dword v62, v[64:65] nt
	v_lshl_add_u64 v[64:65], v[64:65], 0, s[92:93]
	flat_load_dword v63, v[64:65] nt
	v_lshl_add_u64 v[66:67], v[64:65], 0, s[92:93]
	flat_load_dword v64, v[66:67] nt
	v_lshl_add_u64 v[66:67], v[66:67], 0, s[92:93]
	flat_load_dword v65, v[66:67] nt
	v_lshl_add_u64 v[68:69], v[66:67], 0, s[92:93]
	flat_load_dword v66, v[68:69] nt
	v_lshl_add_u64 v[68:69], v[68:69], 0, s[92:93]
	flat_load_dword v67, v[68:69] nt
	v_lshl_add_u64 v[70:71], v[68:69], 0, s[92:93]
	flat_load_dword v68, v[70:71] nt
	v_lshl_add_u64 v[70:71], v[70:71], 0, s[92:93]

.LBB0_585:
	s_cmp_lg_u32 s8, 2
	s_cselect_b32 s35, s34, 0x800
	s_cmp_eq_u32 s8, 1
	s_cselect_b32 s5, s16, s18
	s_cselect_b32 s6, s17, s19
	s_cmp_eq_u32 s8, 0
	s_cselect_b32 s8, s15, s6
	s_cselect_b32 s5, s14, s5
	s_lshl_b32 s6, s34, 11
	s_mul_hi_i32 s7, s11, s6
	s_mul_i32 s6, s11, s6
	s_lshl_b64 s[6:7], s[6:7], 2
	s_add_u32 s6, s5, s6
	v_or_b32_e32 v1, s10, v4
	s_addc_u32 s7, s8, s7
	v_mad_i64_i32 v[8:9], s[8:9], v1, s35, 0
	v_lshl_add_u64 v[8:9], v[8:9], 2, s[6:7]
	s_ashr_i32 s5, s4, 31
	v_lshl_add_u64 v[8:9], s[4:5], 2, v[8:9]
	v_lshlrev_b32_e32 v10, 2, v6
	v_mov_b32_e32 v11, v3
	v_lshl_add_u64 v[8:9], v[8:9], 0, v[10:11]
	s_lshl_b32 s92, s35, 2
	global_load_dword v1, v[8:9], off nt
	v_lshl_add_u64 v[8:9], v[8:9], 0, s[92:93]
	flat_load_dword v5, v[8:9] nt
	v_lshl_add_u64 v[8:9], v[8:9], 0, s[92:93]
	flat_load_dword v7, v[8:9] nt
	v_lshl_add_u64 v[10:11], v[8:9], 0, s[92:93]
	flat_load_dword v8, v[10:11] nt
	v_lshl_add_u64 v[10:11], v[10:11], 0, s[92:93]
	flat_load_dword v9, v[10:11] nt
	v_lshl_add_u64 v[12:13], v[10:11], 0, s[92:93]
	flat_load_dword v10, v[12:13] nt
	v_lshl_add_u64 v[12:13], v[12:13], 0, s[92:93]
	flat_load_dword v11, v[12:13] nt
	v_lshl_add_u64 v[14:15], v[12:13], 0, s[92:93]
	flat_load_dword v12, v[14:15] nt
	v_lshl_add_u64 v[14:15], v[14:15], 0, s[92:93]
	flat_load_dword v13, v[14:15] nt
	v_lshl_add_u64 v[16:17], v[14:15], 0, s[92:93]
	flat_load_dword v14, v[16:17] nt
	v_lshl_add_u64 v[16:17], v[16:17], 0, s[92:93]
	flat_load_dword v15, v[16:17] nt
	v_lshl_add_u64 v[18:19], v[16:17], 0, s[92:93]
	flat_load_dword v16, v[18:19] nt
	v_lshl_add_u64 v[18:19], v[18:19], 0, s[92:93]
	flat_load_dword v17, v[18:19] nt
	v_lshl_add_u64 v[20:21], v[18:19], 0, s[92:93]
	flat_load_dword v18, v[20:21] nt
	v_lshl_add_u64 v[20:21], v[20:21], 0, s[92:93]
	flat_load_dword v19, v[20:21] nt
	v_lshl_add_u64 v[22:23], v[20:21], 0, s[92:93]
	flat_load_dword v20, v[22:23] nt
	v_lshl_add_u64 v[22:23], v[22:23], 0, s[92:93]
	flat_load_dword v21, v[22:23] nt
	v_lshl_add_u64 v[24:25], v[22:23], 0, s[92:93]
	flat_load_dword v22, v[24:25] nt
	v_lshl_add_u64 v[24:25], v[24:25], 0, s[92:93]
	flat_load_dword v23, v[24:25] nt
	v_lshl_add_u64 v[26:27], v[24:25], 0, s[92:93]
	flat_load_dword v24, v[26:27] nt
	v_lshl_add_u64 v[26:27], v[26:27], 0, s[92:93]
	flat_load_dword v25, v[26:27] nt
	v_lshl_add_u64 v[28:29], v[26:27], 0, s[92:93]
	flat_load_dword v26, v[28:29] nt
	v_lshl_add_u64 v[28:29], v[28:29], 0, s[92:93]
	flat_load_dword v27, v[28:29] nt
	v_lshl_add_u64 v[30:31], v[28:29], 0, s[92:93]
	flat_load_dword v28, v[30:31] nt
	v_lshl_add_u64 v[30:31], v[30:31], 0, s[92:93]
	flat_load_dword v29, v[30:31] nt
	v_lshl_add_u64 v[32:33], v[30:31], 0, s[92:93]
	flat_load_dword v30, v[32:33] nt
	v_lshl_add_u64 v[32:33], v[32:33], 0, s[92:93]
	flat_load_dword v31, v[32:33] nt
	v_lshl_add_u64 v[34:35], v[32:33], 0, s[92:93]
	flat_load_dword v32, v[34:35] nt
	v_lshl_add_u64 v[34:35], v[34:35], 0, s[92:93]
	flat_load_dword v33, v[34:35] nt
	v_lshl_add_u64 v[70:71], v[34:35], 0, s[92:93]
	flat_load_dword v34, v[70:71] nt
	v_lshl_add_u64 v[70:71], v[70:71], 0, s[92:93]
	flat_load_dword v35, v[70:71] nt
	v_lshl_add_u64 v[70:71], v[70:71], 0, s[92:93]
	flat_load_dword v36, v[70:71] nt
	v_lshl_add_u64 v[70:71], v[70:71], 0, s[92:93]

; __device__ __forceinline__ unsigned cvt_pk_bf16(float lo, float hi) { const f32x2 v = {lo, hi}; const bf16x2_t b = __builtin_convertvector(v, bf16x2_t); return __builtin_bit_cast(unsigned, b); }
; __device__ __forceinline__ void rwkv_pre_phase(LAS unsigned char* lds, const RwScan& a_, unsigned char* img, const int vcu, const int G, const int tid0_, const bool do_cv, const bool do_work) {
;     ...
;         if (a_xwin && do_cv) {
;             constexpr int XW_NB = (IN_DIM + 31) / 32, XW_TILES = (D / 64) * XW_NB;
;             for (int x = vcu * (NWAVES - PW_NW) + (wave - PW_NW); x < XW_TILES; x += G * (NWAVES - PW_NW)) {
;                 const int kb = x / XW_NB, nb = x - kb * XW_NB, n = nb * 32 + (lane & 31);
;                 if (n < IN_DIM) {
;                     const float* s_ = a_xwin + (size_t)(kb * 64 + 32 * (lane >> 5)) * IN_DIM + n;
;                     float v_[32];
; #pragma unroll
;                     for (int i = 0; i < 32; ++i) v_[i] = s_[(size_t)i * IN_DIM];
;                     bf16_t* d_ = a_xwin_t + (size_t)n * D + kb * 64 + 32 * (lane >> 5);
; #pragma unroll
;                     for (int q = 0; q < 4; ++q) { u32x4 o; o.x = cvt_pk_bf16(v_[8 * q], v_[8 * q + 1]); o.y = cvt_pk_bf16(v_[8 * q + 2], v_[8 * q + 3]); o.z = cvt_pk_bf16(v_[8 * q + 4], v_[8 * q + 5]); o.w = cvt_pk_bf16(v_[8 * q + 6], v_[8 * q + 7]);
;                         *(u32x4*)(d_ + 8 * q) = o; }
;                 }
;             }
.LBB0_604:
	s_mul_hi_i32 s4, s12, 0x2c0b02c1
	s_lshr_b32 s5, s4, 31
	s_ashr_i32 s6, s4, 5
	s_add_i32 s6, s6, s5
	s_mul_i32 s4, s6, 0xffffe8c0
	v_add_u32_e32 v6, s4, v1
	v_cmp_gt_i32_e32 vcc, s68, v6
	s_and_saveexec_b64 s[4:5], vcc
	s_cbranch_execz .LBB0_603
	s_lshl_b32 s6, s6, 6
	v_or_b32_e32 v2, s6, v4
	s_waitcnt lgkmcnt(0)
	v_mov_b64_e32 v[8:9], s[44:45]
	v_mad_i64_i32 v[8:9], s[10:11], v2, s9, v[8:9]
	v_ashrrev_i32_e32 v7, 31, v6
	v_lshl_add_u64 v[8:9], v[6:7], 2, v[8:9]
	v_add_co_u32_e32 v10, vcc, 0x5000, v8
	s_mov_b32 s7, 0x1c000
	s_nop 0
	v_addc_co_u32_e32 v11, vcc, 0, v9, vcc
	global_load_dword v12, v[10:11], off offset:3264
	v_add_co_u32_e32 v10, vcc, 0xb000, v8
	global_load_dword v5, v[8:9], off nt
	s_nop 0
	v_addc_co_u32_e32 v11, vcc, 0, v9, vcc
	global_load_dword v13, v[10:11], off offset:2432
	v_add_co_u32_e32 v10, vcc, 0x11000, v8
	v_lshlrev_b64 v[6:7], 12, v[6:7]
	s_nop 0
	v_addc_co_u32_e32 v11, vcc, 0, v9, vcc
	global_load_dword v14, v[10:11], off offset:1600
	v_add_co_u32_e32 v10, vcc, 0x17000, v8
	v_lshl_add_u64 v[6:7], s[2:3], 0, v[6:7]
	s_nop 0
	v_addc_co_u32_e32 v11, vcc, 0, v9, vcc
	global_load_dword v15, v[10:11], off offset:768
	v_add_co_u32_e32 v10, vcc, s7, v8
	s_ashr_i32 s7, s6, 31
	s_nop 0
	v_addc_co_u32_e32 v11, vcc, 0, v9, vcc
	global_load_dword v16, v[10:11], off offset:4032
	v_add_co_u32_e32 v10, vcc, 0x22000, v8
	v_lshl_add_u64 v[6:7], s[6:7], 1, v[6:7]
	s_nop 0
	v_addc_co_u32_e32 v11, vcc, 0, v9, vcc
	global_load_dword v17, v[10:11], off offset:3200
	v_add_co_u32_e32 v10, vcc, 0x28000, v8
	v_lshlrev_b32_e32 v2, 1, v4
	s_nop 0
	v_addc_co_u32_e32 v11, vcc, 0, v9, vcc
	global_load_dword v18, v[10:11], off offset:2368
	v_add_co_u32_e32 v10, vcc, 0x2e000, v8
	s_nop 1
	v_addc_co_u32_e32 v11, vcc, 0, v9, vcc
	global_load_dword v19, v[10:11], off offset:1536
	v_add_co_u32_e32 v10, vcc, 0x34000, v8
	s_nop 1
	v_addc_co_u32_e32 v11, vcc, 0, v9, vcc
	global_load_dword v20, v[10:11], off offset:704
	v_add_co_u32_e32 v10, vcc, 0x39000, v8
	s_nop 1
	v_addc_co_u32_e32 v11, vcc, 0, v9, vcc
	global_load_dword v21, v[10:11], off offset:3968
	v_add_co_u32_e32 v10, vcc, 0x3f000, v8
	s_nop 1
	v_addc_co_u32_e32 v11, vcc, 0, v9, vcc
	global_load_dword v22, v[10:11], off offset:3136
	v_add_co_u32_e32 v10, vcc, 0x45000, v8
	s_nop 1
	v_addc_co_u32_e32 v11, vcc, 0, v9, vcc
	global_load_dword v23, v[10:11], off offset:2304
	v_add_co_u32_e32 v10, vcc, 0x4b000, v8
	s_nop 1
	v_addc_co_u32_e32 v11, vcc, 0, v9, vcc
	global_load_dword v24, v[10:11], off offset:1472
	v_add_co_u32_e32 v10, vcc, 0x51000, v8
	s_nop 1
	v_addc_co_u32_e32 v11, vcc, 0, v9, vcc
	global_load_dword v25, v[10:11], off offset:640
	v_add_co_u32_e32 v10, vcc, 0x56000, v8
	s_nop 1
	v_addc_co_u32_e32 v11, vcc, 0, v9, vcc
	global_load_dword v26, v[10:11], off offset:3904
	v_add_co_u32_e32 v10, vcc, 0x5c000, v8
	s_nop 1
	v_addc_co_u32_e32 v11, vcc, 0, v9, vcc
	global_load_dword v27, v[10:11], off offset:3072
	v_add_co_u32_e32 v10, vcc, 0x62000, v8
	s_nop 1
	v_addc_co_u32_e32 v11, vcc, 0, v9, vcc
	global_load_dword v28, v[10:11], off offset:2240
	v_add_co_u32_e32 v10, vcc, 0x68000, v8
	s_nop 1
	v_addc_co_u32_e32 v11, vcc, 0, v9, vcc
	global_load_dword v29, v[10:11], off offset:1408
	v_add_co_u32_e32 v10, vcc, 0x6e000, v8
	s_nop 1
	v_addc_co_u32_e32 v11, vcc, 0, v9, vcc
	global_load_dword v30, v[10:11], off offset:576
	v_add_co_u32_e32 v10, vcc, 0x73000, v8
	s_nop 1
	v_addc_co_u32_e32 v11, vcc, 0, v9, vcc
	global_load_dword v31, v[10:11], off offset:3840
	v_add_co_u32_e32 v10, vcc, 0x79000, v8
	s_nop 1
	v_addc_co_u32_e32 v11, vcc, 0, v9, vcc
	global_load_dword v32, v[10:11], off offset:3008
	v_add_co_u32_e32 v10, vcc, 0x7f000, v8
	s_nop 1
	v_addc_co_u32_e32 v11, vcc, 0, v9, vcc
	global_load_dword v33, v[10:11], off offset:2176
	v_add_co_u32_e32 v10, vcc, 0x85000, v8
	s_nop 1
	v_addc_co_u32_e32 v11, vcc, 0, v9, vcc
	global_load_dword v34, v[10:11], off offset:1344
	v_add_co_u32_e32 v10, vcc, 0x8b000, v8
	s_nop 1
	v_addc_co_u32_e32 v11, vcc, 0, v9, vcc
	global_load_dword v35, v[10:11], off offset:512
	v_add_co_u32_e32 v10, vcc, 0x90000, v8
	s_nop 1
	v_addc_co_u32_e32 v11, vcc, 0, v9, vcc
	global_load_dword v36, v[10:11], off offset:3776
	v_add_co_u32_e32 v10, vcc, 0x96000, v8
	s_nop 1
	v_addc_co_u32_e32 v11, vcc, 0, v9, vcc
	global_load_dword v37, v[10:11], off offset:2944
	v_add_co_u32_e32 v10, vcc, 0x9c000, v8
	s_nop 1
	v_addc_co_u32_e32 v11, vcc, 0, v9, vcc
	global_load_dword v38, v[10:11], off offset:2112
	v_add_co_u32_e32 v10, vcc, 0xa2000, v8
	s_nop 1
	v_addc_co_u32_e32 v11, vcc, 0, v9, vcc
	global_load_dword v39, v[10:11], off offset:1280
	v_add_co_u32_e32 v10, vcc, 0xa8000, v8
	s_nop 1
	v_addc_co_u32_e32 v11, vcc, 0, v9, vcc
	global_load_dword v40, v[10:11], off offset:448
	v_add_co_u32_e32 v10, vcc, 0xad000, v8
	s_nop 1
	v_addc_co_u32_e32 v11, vcc, 0, v9, vcc
	v_add_co_u32_e32 v8, vcc, 0xb3000, v8
	global_load_dword v41, v[10:11], off offset:3712
	s_nop 0
	v_addc_co_u32_e32 v9, vcc, 0, v9, vcc
	global_load_dword v42, v[8:9], off offset:2880
	v_lshl_add_u64 v[10:11], v[6:7], 0, v[2:3]
	s_waitcnt vmcnt(30)
	v_cvt_pk_bf16_f32 v6, v5, v12
	s_waitcnt vmcnt(28)
	v_cvt_pk_bf16_f32 v7, v13, v14
	s_waitcnt vmcnt(26)
	v_cvt_pk_bf16_f32 v8, v15, v16
	s_waitcnt vmcnt(24)
	v_cvt_pk_bf16_f32 v9, v17, v18
	global_store_dwordx4 v[10:11], v[6:9], off
	s_waitcnt vmcnt(23)
	s_nop 0
	v_cvt_pk_bf16_f32 v6, v19, v20
	s_waitcnt vmcnt(21)
	v_cvt_pk_bf16_f32 v7, v21, v22
	s_waitcnt vmcnt(19)
	v_cvt_pk_bf16_f32 v8, v23, v24
	s_waitcnt vmcnt(17)
	v_cvt_pk_bf16_f32 v9, v25, v26
	global_store_dwordx4 v[10:11], v[6:9], off offset:16
	s_waitcnt vmcnt(16)
	s_nop 0
	v_cvt_pk_bf16_f32 v6, v27, v28
	s_waitcnt vmcnt(14)
	v_cvt_pk_bf16_f32 v7, v29, v30
	s_waitcnt vmcnt(12)
	v_cvt_pk_bf16_f32 v8, v31, v32
	s_waitcnt vmcnt(10)
	v_cvt_pk_bf16_f32 v9, v33, v34
	global_store_dwordx4 v[10:11], v[6:9], off offset:32
	s_waitcnt vmcnt(9)
	s_nop 0
	v_cvt_pk_bf16_f32 v6, v35, v36
	s_waitcnt vmcnt(7)
	v_cvt_pk_bf16_f32 v7, v37, v38
	s_waitcnt vmcnt(5)
	v_cvt_pk_bf16_f32 v8, v39, v40
	s_waitcnt vmcnt(3)
	v_cvt_pk_bf16_f32 v9, v41, v42
	global_store_dwordx4 v[10:11], v[6:9], off offset:48
	s_branch .LBB0_603
